# s11
# speedup vs baseline: 1.0420x; 1.0160x over previous
_Z11prep_kernelPKfS0_PKiS2_S0_S0_S0_S0_S0_S0_Pc:
	s_lshr_b32 s4, s2, 2
	v_lshrrev_b32_e32 v2, 6, v0
	s_and_b32 s4, s4, 0x1ffffffe
	s_load_dwordx4 s[28:31], s[0:1], 0x40
	s_load_dwordx8 s[12:19], s[0:1], 0x0
	s_load_dwordx8 s[20:27], s[0:1], 0x20
	v_and_b32_e32 v1, 15, v0
	s_and_b32 s3, s2, 7
	v_or_b32_e32 v2, s4, v2
	v_lshl_or_b32 v88, v2, 3, s3
	v_cmp_gt_u32_e64 s[10:11], 14, v1
	v_mul_lo_u32 v7, v88, 14
	v_and_b32_e32 v105, 63, v0
	v_cndmask_b32_e64 v6, 13, v1, s[10:11]
	v_add_u32_e32 v2, v7, v6
	v_mul_u32_u24_e32 v4, 12, v2
	v_lshlrev_b32_e32 v5, 2, v6
	v_cmp_gt_u32_e64 s[8:9], 48, v105
	v_cmp_gt_u32_e64 s[6:7], 14, v105
	v_lshlrev_b32_e32 v118, 1, v0
	v_lshrrev_b32_e32 v104, 4, v0
	v_cndmask_b32_e64 v8, 0, v105, s[8:9]
	v_cndmask_b32_e64 v9, 0, v105, s[6:7]
	v_mad_u32_u24 v8, v88, 48, v8
	v_add_lshl_u32 v9, v7, v9, 2
	v_lshlrev_b32_e32 v8, 2, v8
	s_lshl_b32 s2, s2, 3
	s_and_b32 s2, s2, 0x78
	v_and_b32_e32 v106, 30, v118
	v_or_b32_e32 v107, s2, v104
	v_cmp_gt_u32_e64 s[2:3], 23, v106
	v_or_b32_e32 v10, 1, v106
	v_cmp_gt_u32_e64 s[4:5], 23, v10
	v_lshlrev_b32_e32 v11, 7, v106
	v_lshlrev_b32_e32 v10, 7, v10
	v_cndmask_b32_e64 v11, 0, v11, s[2:3]
	v_cndmask_b32_e64 v10, 0, v10, s[4:5]
	v_or_b32_e32 v11, v11, v107
	v_or_b32_e32 v10, v10, v107
	v_lshlrev_b32_e32 v11, 2, v11
	v_lshlrev_b32_e32 v10, 2, v10
	v_lshlrev_b32_e32 v12, 2, v107
	v_lshlrev_b32_e32 v119, 5, v0
	v_lshlrev_b32_e32 v13, 2, v0
	v_and_b32_e32 v109, 12, v13
	v_and_b32_e32 v91, 0xf80, v119
	v_lshl_or_b32 v91, v109, 2, v91
	v_or_b32_e32 v92, 0x1000, v91
	v_lshlrev_b32_e32 v90, 9, v2
	v_and_b32_e32 v16, 48, v0
	v_or_b32_e32 v90, v90, v16
	v_or_b32_e32 v112, 0x80, v0
	v_or_b32_e32 v111, 0x180, v0
	v_or_b32_e32 v108, 0x280, v0
	v_mov_b32_e32 v87, 0
	v_bfe_u32 v110, v0, 4, 2
	s_waitcnt lgkmcnt(0)
	global_load_dwordx3 v[82:84], v4, s[12:13]
	global_load_dword v85, v5, s[26:27]
	global_load_dword v114, v8, s[18:19]
	global_load_dword v115, v9, s[16:17]
	global_load_dword v116, v11, s[28:29]
	global_load_dword v113, v10, s[28:29]
	global_load_dword v117, v12, s[30:31]
	global_load_dwordx4 v[66:69], v91, s[20:21]
	global_load_dwordx4 v[70:73], v91, s[20:21] offset:64
	global_load_dwordx4 v[74:77], v92, s[20:21]
	global_load_dwordx4 v[78:81], v92, s[20:21] offset:64
	global_load_dwordx4 v[58:61], v91, s[22:23]
	global_load_dwordx4 v[62:65], v91, s[22:23] offset:64
	global_load_dwordx4 v[50:53], v92, s[22:23]
	global_load_dwordx4 v[54:57], v92, s[22:23] offset:64
	global_load_dwordx4 v[42:45], v91, s[24:25]
	global_load_dwordx4 v[46:49], v91, s[24:25] offset:64
	global_load_dwordx4 v[34:37], v92, s[24:25]
	global_load_dwordx4 v[38:41], v92, s[24:25] offset:64
	global_load_dwordx4 v[26:29], v90, s[14:15] nt
	global_load_dwordx4 v[30:33], v90, s[14:15] offset:64 nt
	global_load_dwordx4 v[18:21], v90, s[14:15] offset:128 nt
	global_load_dwordx4 v[22:25], v90, s[14:15] offset:192 nt
	global_load_dwordx4 v[10:13], v90, s[14:15] offset:256 nt
	global_load_dwordx4 v[14:17], v90, s[14:15] offset:320 nt
	global_load_dwordx4 v[2:5], v90, s[14:15] offset:384 nt
	global_load_dwordx4 v[6:9], v90, s[14:15] offset:448 nt
	s_waitcnt vmcnt(26)
	v_mov_b32_e32 v90, v83
	v_mov_b32_e32 v91, v84
	v_lshlrev_b32_e32 v86, 2, v110
	s_waitcnt vmcnt(25)
	v_mul_f32_e32 v84, 0x3fb8aa3b, v85
	s_mov_b32 s14, 0x41700000
	v_exp_f32_e32 v84, v84
	v_cndmask_b32_e64 v94, 0, 1.0, s[10:11]
	v_add_f32_e32 v84, 1.0, v84
	v_cmp_lt_f32_e32 vcc, s14, v85
	v_log_f32_e32 v84, v84
	v_cmp_lt_u32_e64 s[12:13], 15, v105
	v_mul_f32_e32 v84, 0x3f317218, v84
	v_cndmask_b32_e32 v84, v84, v85, vcc
	v_mul_f32_e32 v84, 0xbe715bef, v84
	v_mul_f32_e32 v84, 0x3f3504f3, v84
	v_mul_f32_e32 v84, 0x41800000, v84
	v_cndmask_b32_e64 v99, 0, v84, s[10:11]
	v_mul_f32_e32 v101, -2.0, v99
	v_mov_b32_e32 v95, v101
	v_pk_mul_f32 v[84:85], v[94:95], v[82:83] op_sel:[0,1]
	v_cmp_gt_u32_e32 vcc, 16, v105
	v_mov_b32_e32 v83, v85
	s_and_saveexec_b64 s[14:15], s[12:13]
	s_xor_b64 s[14:15], exec, s[14:15]
	s_cbranch_execz .LBB0_10
	v_pk_mul_f32 v[92:93], v[90:91], v[90:91]
	v_mov_b32_e32 v95, v91
	v_fma_f32 v83, v82, v82, v92
	v_add_f32_e32 v100, v83, v93
	v_pk_mul_f32 v[92:93], v[94:95], v[100:101]
	v_mov_b32_e32 v83, v87
	v_cvt_pk_fp8_f32 v83, v93, 0
	v_mul_f32_e32 v98, v94, v91
	v_cmp_lt_i32_e64 s[12:13], 1, v110
	s_mov_b64 s[16:17], 0
	v_cvt_f32_fp8_e32 v83, v83
	v_sub_f32_e32 v89, v93, v83
	s_and_saveexec_b64 s[18:19], s[12:13]
	s_xor_b64 s[18:19], exec, s[18:19]
	s_cbranch_execz .LBB0_5
	v_cmp_eq_u32_e64 s[12:13], 2, v110
	s_mov_b64 s[20:21], -1
	s_and_saveexec_b64 s[16:17], s[12:13]
	s_cbranch_execz .LBB0_4
	v_mov_b32_e32 v83, 0
	v_mov_b32_e32 v84, 0
	v_mov_b32_e32 v89, 0
	v_cvt_pk_fp8_f32 v84, v99, 0
	v_cvt_pk_fp8_f32 v89, v98, 0
	v_cvt_pk_fp8_f32 v83, v92, 0
	s_xor_b64 s[20:21], exec, -1
	v_cvt_f32_fp8_e32 v85, v84
	v_cvt_f32_fp8_e32 v84, v89
	v_cvt_f32_fp8_e32 v83, v83
	v_mov_b32_e32 v102, v92
	v_pk_add_f32 v[96:97], v[98:99], v[84:85] neg_lo:[0,1] neg_hi:[0,1]
	v_sub_f32_e32 v84, v92, v83
